# v72 + expert gate/up GEMM first unit: the four gathered-row token-id loads issued together (one wait) before the first tile loads
# speedup vs baseline: 1.0047x; 1.0047x over previous
.LBB0_5201:
	s_andn2_b64 vcc, exec, s[4:5]
	s_cbranch_vccnz .LBB0_5252
	v_bfe_i32 v2, v6, 27, 1
	v_lshlrev_b32_e32 v7, 4, v6
	v_lshrrev_b32_e32 v2, 22, v2
	s_add_u32 s4, s10, 0x15c00000
	v_ashrrev_i32_e32 v0, 31, v6
	v_add_u32_e32 v2, v7, v2
	s_addc_u32 s5, s11, 0
	v_lshrrev_b32_e32 v0, 26, v0
	v_and_b32_e32 v2, 0xfffffc00, v2
	s_lshl_b32 s6, s64, 2
	v_add_u32_e32 v0, v6, v0
	v_sub_u32_e32 v2, v7, v2
	s_add_i32 s13, s6, 0
	v_ashrrev_i32_e32 v0, 6, v0
	v_lshrrev_b32_e32 v3, 4, v2
	s_add_i32 s13, s13, 0x20200
	v_bitop3_b32 v3, v3, v2, 32 bitop3:0x6c
	v_lshlrev_b32_e32 v2, 3, v0
	v_mov_b32_e32 v5, s13
	v_and_b32_e32 v4, -16, v2
	v_ashrrev_i32_e32 v2, 31, v3
	ds_read_b32 v5, v5 offset:68
	v_lshrrev_b32_e32 v2, 26, v2
	v_add_u32_e32 v2, v3, v2
	v_ashrrev_i32_e32 v2, 6, v2
	v_add_u32_e32 v242, v2, v4
	s_lshl_b32 s14, s65, 8
	v_add_u32_e32 v8, s14, v242
	s_waitcnt lgkmcnt(0)
	v_readfirstlane_b32 s6, v5
	s_lshl_b32 s12, s64, 14
	v_mov_b32_e32 v5, 0
	v_cmp_gt_i32_e32 vcc, s6, v8
	v_mov_b32_e32 v4, 0
	s_and_saveexec_b64 s[6:7], vcc
	s_cbranch_execz .LBB0_5204
	v_add_u32_e32 v8, s12, v8
	v_ashrrev_i32_e32 v9, 31, v8
	v_lshl_add_u64 v[8:9], v[8:9], 2, s[4:5]
	global_load_dword v4, v[8:9], off
.LBB0_5204:
	s_or_b64 exec, exec, s[6:7]
	v_mov_b32_e32 v9, s13
	ds_read_b32 v9, v9 offset:68
	v_add_u32_e32 v243, 0x80, v242
	v_add_u32_e32 v8, s14, v243
	s_waitcnt lgkmcnt(0)
	v_readfirstlane_b32 s6, v9
	s_nop 1
	v_cmp_gt_i32_e32 vcc, s6, v8
	s_and_saveexec_b64 s[6:7], vcc
	s_cbranch_execz .LBB0_5206
	v_add_u32_e32 v8, s12, v8
	v_ashrrev_i32_e32 v9, 31, v8
	v_lshl_add_u64 v[8:9], v[8:9], 2, s[4:5]
	global_load_dword v5, v[8:9], off
.LBB0_5206:
	s_or_b64 exec, exec, s[6:7]
	v_add_u32_e32 v7, 0x2000, v7
	v_ashrrev_i32_e32 v8, 31, v7
	v_lshrrev_b32_e32 v8, 22, v8
	v_add_u32_e32 v8, v7, v8
	v_ashrrev_i32_e32 v9, 10, v8
	v_mul_i32_i24_e32 v8, 0x400, v9
	v_sub_u32_e32 v7, v7, v8
	v_lshrrev_b32_e32 v8, 4, v7
	v_bitop3_b32 v10, v8, v7, 32 bitop3:0x6c
	v_lshlrev_b32_e32 v7, 3, v9
	v_mov_b32_e32 v11, s13
	v_and_b32_e32 v8, -16, v7
	v_ashrrev_i32_e32 v7, 31, v10
	ds_read_b32 v11, v11 offset:68
	v_lshrrev_b32_e32 v7, 26, v7
	v_add_u32_e32 v7, v10, v7
	v_ashrrev_i32_e32 v7, 6, v7
	v_add_u32_e32 v244, v7, v8
	v_add_u32_e32 v12, s14, v244
	s_waitcnt lgkmcnt(0)
	v_readfirstlane_b32 s6, v11
	v_mov_b32_e32 v8, 0
	v_mov_b32_e32 v11, 0
	v_cmp_gt_i32_e32 vcc, s6, v12
	s_and_saveexec_b64 s[6:7], vcc
	s_cbranch_execz .LBB0_5208
	v_add_u32_e32 v12, s12, v12
	v_ashrrev_i32_e32 v13, 31, v12
	v_lshl_add_u64 v[12:13], v[12:13], 2, s[4:5]
	global_load_dword v11, v[12:13], off
.LBB0_5208:
	s_or_b64 exec, exec, s[6:7]
	v_mov_b32_e32 v13, s13
	ds_read_b32 v13, v13 offset:68
	v_add_u32_e32 v245, 0x80, v244
	v_add_u32_e32 v12, s14, v245
	s_waitcnt lgkmcnt(0)
	v_readfirstlane_b32 s6, v13
	s_nop 1
	v_cmp_gt_i32_e32 vcc, s6, v12
	s_and_saveexec_b64 s[6:7], vcc
	s_cbranch_execz .LBB0_5210
	v_add_u32_e32 v12, s12, v12
	v_ashrrev_i32_e32 v13, 31, v12
	v_lshl_add_u64 v[12:13], v[12:13], 2, s[4:5]
	global_load_dword v8, v[12:13], off
.LBB0_5210:
	s_or_b64 exec, exec, s[6:7]
	s_waitcnt vmcnt(0)
	v_lshlrev_b32_e32 v4, 11, v4
	v_lshlrev_b32_e32 v5, 11, v5
	v_lshlrev_b32_e32 v11, 11, v11
	v_lshlrev_b32_e32 v8, 11, v8
	v_lshlrev_b32_e32 v12, 6, v7
	v_sub_u32_e32 v10, v10, v12
	v_lshlrev_b32_e32 v9, 5, v9
	v_ashrrev_i16_sdwa v10, v228, sext(v10) dst_sel:DWORD dst_unused:UNUSED_PAD src0_sel:DWORD src1_sel:BYTE_0
	v_and_b32_e32 v9, 32, v9
	v_bfe_i32 v10, v10, 0, 16
	v_add_lshl_u32 v246, v9, v10, 1
	v_lshlrev_b32_e32 v9, 6, v2
	s_lshl_b32 s12, s48, 26
	v_sub_u32_e32 v3, v3, v9
	s_add_u32 s6, s10, 0x38400000
	v_lshlrev_b32_e32 v0, 5, v0
	v_ashrrev_i16_sdwa v3, v228, sext(v3) dst_sel:DWORD dst_unused:UNUSED_PAD src0_sel:DWORD src1_sel:BYTE_0
	s_addc_u32 s7, s11, 0
	v_and_b32_e32 v0, 32, v0
	v_bfe_i32 v3, v3, 0, 16
	s_add_u32 s12, s10, s12
	v_add_lshl_u32 v247, v0, v3, 1
	s_addc_u32 s13, s11, 0
	v_add_u32_e32 v204, v4, v247
	s_add_u32 s44, s12, 0x8e00000
	v_lshlrev_b32_e32 v3, 1, v242
	v_lshrrev_b32_e32 v4, 2, v242
	v_and_b32_e32 v2, 3, v2
	s_mov_b32 s12, 0x1fffe0
	v_and_b32_e32 v3, 24, v3
	v_and_b32_e32 v4, 4, v4
	v_and_or_b32 v2, v242, s12, v2
	s_addc_u32 s45, s13, 0
	v_or3_b32 v2, v2, v4, v3
	v_and_b32_e32 v4, 3, v7
	s_ashr_i32 s21, s22, 6
	s_ashr_i32 s31, s30, 31
	s_ashr_i32 s20, s22, 8
	v_and_or_b32 v4, v244, s12, v4
	s_lshl_b32 s46, s21, 10
	s_lshl_b64 s[12:13], s[30:31], 19
	s_add_u32 s34, s44, s12
	v_lshl_add_u32 v198, v2, 11, v247
	v_lshlrev_b32_e32 v2, 1, v244
	v_lshrrev_b32_e32 v3, 2, v244
	s_addc_u32 s35, s45, s13
	s_add_i32 s31, s46, 0
	v_and_b32_e32 v2, 24, v2
	v_and_b32_e32 v3, 4, v3
	s_add_i32 s47, s31, 0x10000
	s_add_i32 s48, s31, 0x12000
	v_or3_b32 v2, v4, v3, v2
	s_mov_b32 m0, s47
	s_add_u32 s12, s34, 0x40000
	v_lshl_add_u32 v200, v2, 11, v246
	global_load_lds_dwordx4 v198, s[34:35]
	s_mov_b32 m0, s48
	s_addc_u32 s13, s35, 0
	s_add_i32 s49, s31, 0x14000
	global_load_lds_dwordx4 v200, s[34:35]
	s_mov_b32 m0, s49
	s_add_i32 s50, s31, 0x16000
	global_load_lds_dwordx4 v198, s[12:13]
	s_mov_b32 m0, s50
	s_add_i32 s51, s31, 0x2000
	global_load_lds_dwordx4 v200, s[12:13]
	s_mov_b32 m0, s31
	v_add_u32_e32 v202, v11, v246
	global_load_lds_dwordx4 v204, s[6:7]
	s_mov_b32 m0, s51
	s_add_i32 s52, s31, 0x4000
	v_add_u32_e32 v0, v5, v247
	global_load_lds_dwordx4 v202, s[6:7]
	s_mov_b32 m0, s52
	s_add_i32 s53, s31, 0x6000
	v_add_u32_e32 v206, v8, v246
	global_load_lds_dwordx4 v0, s[6:7]
	s_mov_b32 m0, s53
	v_mov_b32_e32 v199, v1
	global_load_lds_dwordx4 v206, s[6:7]
	v_mov_b32_e32 v201, v1
	s_cmp_eq_u32 s20, 1
	v_lshl_add_u64 v[2:3], s[34:35], 0, v[198:199]
	s_cselect_b64 s[12:13], -1, 0
	s_cmp_lg_u32 s20, 1
	v_lshl_add_u64 v[4:5], s[34:35], 0, v[200:201]
	s_cbranch_scc1 .LBB0_5212
	s_barrier
